# layout
# speedup vs baseline: 1.0251x; 1.0042x over previous
_Z11attn_kernelILi4EEvPKfS1_S1_S1_S1_S1_PKcPf:
	s_load_dwordx2 s[24:25], s[0:1], 0x30
	s_load_dwordx8 s[8:15], s[0:1], 0x0
	s_load_dwordx4 s[16:19], s[0:1], 0x20
	v_lshrrev_b32_e32 v63, 6, v0
	v_and_b32_e32 v57, 15, v0
	v_bfe_u32 v1, v0, 4, 2
	v_lshrrev_b32_e32 v2, 2, v57
	v_mul_u32_u24_e32 v4, 3, v1
	v_mul_u32_u24_e32 v2, 3, v2
	v_mad_u32_u24 v4, v63, 12, v4
	v_mad_u32_u24 v2, v63, 12, v2
	v_lshlrev_b32_e32 v4, 2, v4
	v_lshlrev_b32_e32 v2, 2, v2
	v_and_b32_e32 v104, 63, v0
	v_lshlrev_b32_e32 v60, 5, v57
	v_lshlrev_b32_e32 v58, 3, v1
	v_add_u32_e32 v3, v60, v58
	v_lshrrev_b32_e32 v56, 4, v0
	v_lshlrev_b32_e32 v54, 4, v57
	v_mov_b32_e32 v59, 0
	s_movk_i32 s4, 0xe0
	v_cmp_gt_u32_e64 s[4:5], s4, v0
	s_lshl_b32 s26, s2, 8
	s_lshl_b32 s27, s2, 9
	s_mul_i32 s28, s2, 14
	s_add_u32 s26, s26, 0x164000
	s_add_u32 s27, s27, 0x80000
	s_add_u32 s20, s26, 0xc0
	v_lshlrev_b32_e32 v5, 2, v57
	v_lshlrev_b32_e32 v147, 6, v57
	v_add_u32_e32 v2, s26, v2
	v_add_u32_e32 v4, s26, v4
	v_add_u32_e32 v3, s27, v3
	v_mul_u32_u24_e32 v156, 0x140, v1
	s_movk_i32 s21, 0x500
	v_mad_u32_u24 v156, v63, s21, v156
	v_lshl_or_b32 v156, v57, 2, v156
	v_add_u32_e32 v156, 0x1c00, v156
	v_lshlrev_b32_e32 v157, 5, v56
	v_cmp_gt_u32_e32 vcc, 3, v57
	v_add_u32_e32 v158, 4, v57
	v_lshlrev_b32_e32 v159, 2, v57
	s_movk_i32 s21, 0x50
	v_cndmask_b32_e32 v158, 4, v158, vcc
	v_mad_u32_u24 v159, v56, s21, v159
	v_lshl_add_u32 v158, v158, 2, v157
	v_mul_u32_u24_e32 v250, 0x50, v56
	v_or_b32_e32 v250, 0x3800, v250
	v_lshl_add_u32 v251, v57, 1, v250
	v_mul_u32_u24_e32 v252, 0x50, v57
	v_lshl_add_u32 v252, v58, 1, v252
	v_lshlrev_b32_e32 v253, 2, v57
	v_and_b32_e32 v254, 0xc0, v0
	v_lshlrev_b32_e32 v255, 11, v1
	v_or3_b32 v253, v253, v254, v255
	v_add_u32_e32 v254, s28, v56
	v_lshl_add_u32 v254, v254, 9, v54
	v_lshl_or_b32 v255, v56, 9, v54
	s_waitcnt lgkmcnt(0)
	global_load_dwordx3 v[80:82], v2, s[24:25]
	global_load_dwordx3 v[84:86], v4, s[24:25]
	global_load_dwordx2 v[64:65], v3, s[24:25]
	s_load_dword s3, s[24:25], s20
	s_add_u32 s22, s24, 0x160000
	s_addc_u32 s23, s25, 0
	v_cndmask_b32_e64 v62, 13, v56, s[4:5]
	v_add_u32_e32 v3, s28, v62
	v_mad_u32_u24 v144, v3, 36, v5
	v_mad_u32_u24 v146, v3, 12, v5
	v_add_u32_e32 v145, -36, v146
	v_add_u32_e32 v146, -48, v146
	v_lshl_or_b32 v147, v63, 10, v147
	v_lshl_or_b32 v147, v1, 4, v147
	v_or_b32_e32 v148, 0x1000, v147
	v_lshlrev_b32_e32 v149, 4, v104
	v_lshlrev_b32_e32 v150, 9, v3
	v_add_u32_e32 v150, v150, v54
	v_and_b32_e32 v87, 3, v57
	v_lshlrev_b32_e32 v87, 4, v87
	v_lshl_or_b32 v87, v1, 6, v87
	v_lshlrev_b32_e32 v88, 3, v57
	s_add_u32 s26, s24, 0x100000
	s_addc_u32 s27, s25, 0
	s_add_u32 s28, s24, 0x140000
	s_addc_u32 s29, s25, 0
	s_movk_i32 s6, 0x140
	v_cmp_gt_u32_e32 vcc, s6, v0
	v_lshlrev_b32_e32 v22, 2, v0
	v_mov_b32_e32 v23, 0
	s_and_saveexec_b64 s[6:7], vcc
	ds_write_b32 v22, v23 offset:14336
	s_or_b64 exec, exec, s[6:7]
	v_cmp_gt_u32_e32 vcc, 64, v0
	s_and_saveexec_b64 s[6:7], vcc
	ds_write_b32 v22, v23 offset:15360
	s_or_b64 exec, exec, s[6:7]
	v_mov_b32_e32 v45, 0xc9c35000
	s_mov_b32 s30, 0x3db8aa3b
	s_mov_b32 s31, 0x3db8aa3b
	v_mov_b32_e32 v121, 0x3fb8aa3b
	v_mov_b32_e32 v35, 0
	v_mov_b32_e32 v44, v45
	s_waitcnt lgkmcnt(0)
	s_bitcmp0_b32 s3, 1
	s_cselect_b64 s[20:21], -1, 0
	s_cbranch_scc1 .LBB1_16
	v_bfe_u32 v46, s3, v57, 1
	v_cmp_eq_u32_e32 vcc, 0, v46
	s_nop 1
	v_cndmask_b32_e32 v47, 0, v45, vcc
	v_cndmask_b32_e64 v55, 1.0, 0, vcc
	s_nop 0
	v_mov_b32_dpp v34, v47 row_newbcast:0 row_mask:0xf bank_mask:0xf bound_ctrl:1
	v_mov_b32_dpp v36, v47 row_newbcast:2 row_mask:0xf bank_mask:0xf bound_ctrl:1
	v_mov_b32_dpp v37, v47 row_newbcast:3 row_mask:0xf bank_mask:0xf bound_ctrl:1
	v_mov_b32_dpp v22, v47 row_newbcast:4 row_mask:0xf bank_mask:0xf bound_ctrl:1
	v_mov_b32_dpp v23, v47 row_newbcast:5 row_mask:0xf bank_mask:0xf bound_ctrl:1
	v_mov_b32_dpp v24, v47 row_newbcast:6 row_mask:0xf bank_mask:0xf bound_ctrl:1
	v_mov_b32_dpp v25, v47 row_newbcast:7 row_mask:0xf bank_mask:0xf bound_ctrl:1
	v_mov_b32_dpp v38, v47 row_newbcast:8 row_mask:0xf bank_mask:0xf bound_ctrl:1
	v_mov_b32_dpp v39, v47 row_newbcast:9 row_mask:0xf bank_mask:0xf bound_ctrl:1
	v_mov_b32_dpp v40, v47 row_newbcast:10 row_mask:0xf bank_mask:0xf bound_ctrl:1
	v_mov_b32_dpp v41, v47 row_newbcast:11 row_mask:0xf bank_mask:0xf bound_ctrl:1
	v_mov_b32_dpp v42, v47 row_newbcast:12 row_mask:0xf bank_mask:0xf bound_ctrl:1
	v_mov_b32_dpp v43, v47 row_newbcast:13 row_mask:0xf bank_mask:0xf bound_ctrl:1
	s_waitcnt vmcnt(1)
	v_lshl_add_u32 v72, v80, 9, v87
	v_lshl_add_u32 v73, v81, 9, v87
	v_lshl_add_u32 v74, v82, 9, v87
	global_load_dwordx4 v[50:53], v72, s[24:25]
	global_load_dwordx4 v[46:49], v72, s[24:25] offset:256
	global_load_dwordx4 v[14:17], v73, s[24:25]
	global_load_dwordx4 v[10:13], v73, s[24:25] offset:256
	global_load_dwordx4 v[6:9], v74, s[24:25]
	global_load_dwordx4 v[2:5], v74, s[24:25] offset:256
	v_lshl_add_u32 v75, v84, 8, v54
	v_lshl_add_u32 v78, v84, 7, v88
	v_lshl_add_u32 v76, v85, 8, v54
	v_lshl_add_u32 v79, v85, 7, v88
	v_lshl_add_u32 v77, v86, 8, v54
	v_lshl_add_u32 v80, v86, 7, v88
	global_load_dwordx4 v[30:33], v75, s[26:27]
	global_load_dwordx2 v[70:71], v78, s[28:29]
	global_load_dwordx4 v[26:29], v76, s[26:27]
	global_load_dwordx2 v[66:67], v79, s[28:29]
	global_load_dwordx4 v[18:21], v77, s[26:27]
	global_load_dwordx2 v[68:69], v80, s[28:29]
	s_mov_b32 exec_lo, 0x1ff01ff
	s_mov_b32 exec_hi, 0x1ff01ff
	global_load_dword v120, v144, s[10:11]
	s_mov_b32 exec_lo, 0xe000e00
	s_mov_b32 exec_hi, 0xe000e00
	global_load_dword v120, v145, s[12:13]
	s_mov_b32 exec_lo, 0x70007000
	s_mov_b32 exec_hi, 0x70007000
	global_load_dword v120, v146, s[14:15]
	s_mov_b64 exec, -1
	global_load_dwordx4 v[124:127], v147, s[22:23]
	global_load_dwordx4 v[128:131], v148, s[22:23]
	s_mov_b32 exec_hi, 0
	global_load_dwordx4 v[132:135], v149, s[16:17]
	s_mov_b32 exec_hi, -1
	s_mov_b32 exec_lo, 0
	global_load_dwordx4 v[132:135], v149, s[18:19] offset:-512
	s_mov_b32 exec_lo, -1
	global_load_dwordx4 v[136:139], v150, s[8:9]
	global_load_dwordx4 v[140:143], v150, s[8:9] offset:256
	v_mov_b32_e32 v75, 0
	v_mov_b32_e32 v79, 0
	v_mov_b32_e32 v83, 0
	s_waitcnt vmcnt(20)
	v_mfma_f32_16x16x32_fp8_fp8 v[160:163], v[50:51], v[64:65], v[34:37]
	v_mfma_f32_16x16x32_fp8_fp8 v[164:167], v[52:53], v[64:65], v[22:25]
	s_waitcnt vmcnt(19)
	v_mfma_f32_16x16x32_fp8_fp8 v[168:171], v[46:47], v[64:65], v[38:41]
	v_mfma_f32_16x16x32_fp8_fp8 v[172:175], v[48:49], v[64:65], v[42:45]
	s_nop 3
	v_max3_f32 v86, v160, v161, v162
	v_max3_f32 v87, v163, v164, v165
	v_max3_f32 v88, v166, v167, v168
	v_max3_f32 v89, v169, v170, v171
	v_max3_f32 v86, v86, v172, v173
	v_max3_f32 v87, v87, v88, v89
	v_max_f32_e32 v96, v86, v87
	v_mul_f32_e32 v98, 0xbdb8aa3b, v96
	v_pk_fma_f32 v[208:209], v[160:161], s[30:31], v[98:99] op_sel_hi:[1,1,0]
	v_pk_fma_f32 v[210:211], v[162:163], s[30:31], v[98:99] op_sel_hi:[1,1,0]
	v_pk_fma_f32 v[212:213], v[164:165], s[30:31], v[98:99] op_sel_hi:[1,1,0]
	v_pk_fma_f32 v[214:215], v[166:167], s[30:31], v[98:99] op_sel_hi:[1,1,0]
	v_pk_fma_f32 v[216:217], v[168:169], s[30:31], v[98:99] op_sel_hi:[1,1,0]
	v_pk_fma_f32 v[218:219], v[170:171], s[30:31], v[98:99] op_sel_hi:[1,1,0]
	v_pk_fma_f32 v[220:221], v[172:173], s[30:31], v[98:99] op_sel_hi:[1,1,0]
	v_exp_f32_e32 v208, v208
	v_exp_f32_e32 v209, v209
	v_exp_f32_e32 v210, v210
	v_exp_f32_e32 v211, v211
	v_exp_f32_e32 v212, v212
	v_exp_f32_e32 v213, v213
	v_exp_f32_e32 v214, v214
	v_exp_f32_e32 v215, v215
	v_exp_f32_e32 v216, v216
	v_exp_f32_e32 v217, v217
	v_exp_f32_e32 v218, v218
	v_exp_f32_e32 v219, v219
	v_exp_f32_e32 v220, v220
	v_exp_f32_e32 v221, v221
	s_waitcnt vmcnt(18)
	v_mfma_f32_16x16x32_fp8_fp8 v[176:179], v[14:15], v[64:65], v[34:37]
	v_mfma_f32_16x16x32_fp8_fp8 v[180:183], v[16:17], v[64:65], v[22:25]
	s_waitcnt vmcnt(17)
	v_mfma_f32_16x16x32_fp8_fp8 v[184:187], v[10:11], v[64:65], v[38:41]
	v_mfma_f32_16x16x32_fp8_fp8 v[188:191], v[12:13], v[64:65], v[42:45]
	v_pk_add_f32 v[86:87], v[208:209], v[210:211]
	v_pk_add_f32 v[88:89], v[212:213], v[214:215]
	v_pk_add_f32 v[90:91], v[216:217], v[218:219]
	v_pk_mul_f32 v[92:93], v[208:209], v[160:161]
	v_pk_mul_f32 v[94:95], v[210:211], v[162:163]
	v_pk_add_f32 v[86:87], v[86:87], v[220:221]
	v_pk_add_f32 v[88:89], v[88:89], v[90:91]
	v_pk_fma_f32 v[92:93], v[212:213], v[164:165], v[92:93]
	v_pk_fma_f32 v[94:95], v[214:215], v[166:167], v[94:95]
	v_pk_add_f32 v[86:87], v[86:87], v[88:89]
	v_pk_fma_f32 v[92:93], v[216:217], v[168:169], v[92:93]
	v_pk_fma_f32 v[94:95], v[218:219], v[170:171], v[94:95]
	v_add_f32_e32 v86, v86, v87
	v_pk_fma_f32 v[92:93], v[220:221], v[172:173], v[92:93]
	v_rcp_f32_e32 v87, v86
	v_pk_add_f32 v[92:93], v[92:93], v[94:95]
	v_mul_f32_e32 v87, v55, v87
	v_add_f32_e32 v92, v92, v93
	v_mul_f32_e32 v107, v86, v87
	v_mul_f32_e32 v92, v92, v87
	v_mul_f32_e32 v100, 0x43800000, v87
	v_mul_f32_e32 v103, 0x3d800000, v92
	v_max3_f32 v86, v176, v177, v178
	v_max3_f32 v87, v179, v180, v181
	v_max3_f32 v88, v182, v183, v184
	v_max3_f32 v89, v185, v186, v187
	v_max3_f32 v86, v86, v188, v189
	v_max3_f32 v87, v87, v88, v89
	v_max_f32_e32 v96, v86, v87
	v_mul_f32_e32 v98, 0xbdb8aa3b, v96
	v_pk_fma_f32 v[222:223], v[176:177], s[30:31], v[98:99] op_sel_hi:[1,1,0]
	v_pk_fma_f32 v[224:225], v[178:179], s[30:31], v[98:99] op_sel_hi:[1,1,0]
	v_pk_fma_f32 v[226:227], v[180:181], s[30:31], v[98:99] op_sel_hi:[1,1,0]
	v_pk_fma_f32 v[228:229], v[182:183], s[30:31], v[98:99] op_sel_hi:[1,1,0]
	v_pk_fma_f32 v[230:231], v[184:185], s[30:31], v[98:99] op_sel_hi:[1,1,0]
	v_pk_fma_f32 v[232:233], v[186:187], s[30:31], v[98:99] op_sel_hi:[1,1,0]
	v_pk_fma_f32 v[234:235], v[188:189], s[30:31], v[98:99] op_sel_hi:[1,1,0]
	v_exp_f32_e32 v222, v222
	v_exp_f32_e32 v223, v223
	v_exp_f32_e32 v224, v224
	v_exp_f32_e32 v225, v225
	v_exp_f32_e32 v226, v226
	v_exp_f32_e32 v227, v227
	v_exp_f32_e32 v228, v228
	v_exp_f32_e32 v229, v229
	v_exp_f32_e32 v230, v230
	v_exp_f32_e32 v231, v231
	v_exp_f32_e32 v232, v232
	v_exp_f32_e32 v233, v233
	v_exp_f32_e32 v234, v234
	v_exp_f32_e32 v235, v235
	s_waitcnt vmcnt(16)
	v_mfma_f32_16x16x32_fp8_fp8 v[192:195], v[6:7], v[64:65], v[34:37]
	v_mfma_f32_16x16x32_fp8_fp8 v[196:199], v[8:9], v[64:65], v[22:25]
	s_waitcnt vmcnt(15)
	v_mfma_f32_16x16x32_fp8_fp8 v[200:203], v[2:3], v[64:65], v[38:41]
	v_mfma_f32_16x16x32_fp8_fp8 v[204:207], v[4:5], v[64:65], v[42:45]
	v_pk_add_f32 v[86:87], v[222:223], v[224:225]
	v_pk_add_f32 v[88:89], v[226:227], v[228:229]
	v_pk_add_f32 v[90:91], v[230:231], v[232:233]
	v_pk_mul_f32 v[92:93], v[222:223], v[176:177]
	v_pk_mul_f32 v[94:95], v[224:225], v[178:179]
	v_pk_add_f32 v[86:87], v[86:87], v[234:235]
	v_pk_add_f32 v[88:89], v[88:89], v[90:91]
	v_pk_fma_f32 v[92:93], v[226:227], v[180:181], v[92:93]
	v_pk_fma_f32 v[94:95], v[228:229], v[182:183], v[94:95]
	v_pk_add_f32 v[86:87], v[86:87], v[88:89]
	v_pk_fma_f32 v[92:93], v[230:231], v[184:185], v[92:93]
	v_pk_fma_f32 v[94:95], v[232:233], v[186:187], v[94:95]
	v_add_f32_e32 v86, v86, v87
	v_pk_fma_f32 v[92:93], v[234:235], v[188:189], v[92:93]
	v_rcp_f32_e32 v87, v86
	v_pk_add_f32 v[92:93], v[92:93], v[94:95]
	v_mul_f32_e32 v87, v55, v87
	v_add_f32_e32 v92, v92, v93
	v_mul_f32_e32 v108, v86, v87
	v_mul_f32_e32 v92, v92, v87
	v_mul_f32_e32 v101, 0x43800000, v87
	v_mul_f32_e32 v105, 0x3d800000, v92
	v_max3_f32 v86, v192, v193, v194
	v_max3_f32 v87, v195, v196, v197
	v_max3_f32 v88, v198, v199, v200
	v_max3_f32 v89, v201, v202, v203
	v_max3_f32 v86, v86, v204, v205
	v_max3_f32 v87, v87, v88, v89
	v_max_f32_e32 v96, v86, v87
	v_mul_f32_e32 v98, 0xbdb8aa3b, v96
	v_pk_fma_f32 v[236:237], v[192:193], s[30:31], v[98:99] op_sel_hi:[1,1,0]
	v_pk_fma_f32 v[238:239], v[194:195], s[30:31], v[98:99] op_sel_hi:[1,1,0]
	v_pk_fma_f32 v[240:241], v[196:197], s[30:31], v[98:99] op_sel_hi:[1,1,0]
	v_pk_fma_f32 v[242:243], v[198:199], s[30:31], v[98:99] op_sel_hi:[1,1,0]
	v_pk_fma_f32 v[244:245], v[200:201], s[30:31], v[98:99] op_sel_hi:[1,1,0]
	v_pk_fma_f32 v[246:247], v[202:203], s[30:31], v[98:99] op_sel_hi:[1,1,0]
	v_pk_fma_f32 v[248:249], v[204:205], s[30:31], v[98:99] op_sel_hi:[1,1,0]
	v_exp_f32_e32 v236, v236
	v_exp_f32_e32 v237, v237
	v_exp_f32_e32 v238, v238
	v_exp_f32_e32 v239, v239
	v_exp_f32_e32 v240, v240
	v_exp_f32_e32 v241, v241
	v_exp_f32_e32 v242, v242
	v_exp_f32_e32 v243, v243
	v_exp_f32_e32 v244, v244
	v_exp_f32_e32 v245, v245
	v_exp_f32_e32 v246, v246
	v_exp_f32_e32 v247, v247
	v_exp_f32_e32 v248, v248
	v_exp_f32_e32 v249, v249
	v_pk_add_f32 v[86:87], v[236:237], v[238:239]
	v_pk_add_f32 v[88:89], v[240:241], v[242:243]
	v_pk_add_f32 v[90:91], v[244:245], v[246:247]
	v_pk_mul_f32 v[92:93], v[236:237], v[192:193]
	v_pk_mul_f32 v[94:95], v[238:239], v[194:195]
	v_pk_add_f32 v[86:87], v[86:87], v[248:249]
	v_pk_add_f32 v[88:89], v[88:89], v[90:91]
	v_pk_fma_f32 v[92:93], v[240:241], v[196:197], v[92:93]
	v_pk_fma_f32 v[94:95], v[242:243], v[198:199], v[94:95]
	v_pk_add_f32 v[86:87], v[86:87], v[88:89]
	v_pk_fma_f32 v[92:93], v[244:245], v[200:201], v[92:93]
	v_pk_fma_f32 v[94:95], v[246:247], v[202:203], v[94:95]
	v_add_f32_e32 v86, v86, v87
	v_pk_fma_f32 v[92:93], v[248:249], v[204:205], v[92:93]
	v_rcp_f32_e32 v87, v86
	v_pk_add_f32 v[92:93], v[92:93], v[94:95]
	v_mul_f32_e32 v87, v55, v87
	v_add_f32_e32 v92, v92, v93
	v_mul_f32_e32 v109, v86, v87
	v_mul_f32_e32 v92, v92, v87
	v_mul_f32_e32 v102, 0x43800000, v87
	v_mul_f32_e32 v106, 0x3d800000, v92
	v_max3_f32 v122, v103, v105, v106
	v_cmp_gt_u32_e64 s[6:7], 16, v104
	v_mov_b32_e32 v123, v122
	s_nop 1
	v_permlane16_swap_b32_e32 v122, v123
	v_max_f32_e32 v122, v122, v123
	v_mov_b32_e32 v123, v122
	s_nop 1
	v_permlane32_swap_b32_e32 v122, v123
	v_max_f32_e32 v36, v122, v123
	v_mul_f32_e32 v123, 0x3fb8aa3b, v36
	v_fma_f32 v111, v103, v121, -v123
	v_exp_f32_e32 v111, v111
	s_nop 0
	v_mul_f32_e32 v112, v111, v100
	v_mul_f32_e32 v110, v111, v107
	v_mov_b32_e32 v114, v111
	v_pk_mul_f32 v[208:209], v[208:209], v[112:113] op_sel_hi:[1,0]
	v_pk_mul_f32 v[210:211], v[210:211], v[112:113] op_sel_hi:[1,0]
	v_pk_mul_f32 v[212:213], v[212:213], v[112:113] op_sel_hi:[1,0]
	v_pk_mul_f32 v[214:215], v[214:215], v[112:113] op_sel_hi:[1,0]
	v_pk_mul_f32 v[216:217], v[216:217], v[112:113] op_sel_hi:[1,0]
	v_pk_mul_f32 v[218:219], v[218:219], v[112:113] op_sel_hi:[1,0]
	v_pk_mul_f32 v[220:221], v[220:221], v[112:113] op_sel_hi:[1,0]
	s_waitcnt vmcnt(13)
	v_mov_b32_e32 v115, v110
	v_fma_mix_f32 v116, v110, v70, 0 op_sel_hi:[0,1,0]
	v_fma_mix_f32 v117, v110, v70, 0 op_sel:[0,1,0] op_sel_hi:[0,1,0]
	v_fma_mix_f32 v118, v110, v71, 0 op_sel_hi:[0,1,0]
	v_cvt_pk_fp8_f32 v72, v208, v209
	v_cvt_pk_fp8_f32 v73, v212, v213
	v_cvt_pk_fp8_f32 v74, v216, v217
	v_cvt_pk_fp8_f32 v75, v220, v221
	v_cvt_pk_fp8_f32 v72, v210, v211 op_sel:[0,0,1]
	v_cvt_pk_fp8_f32 v73, v214, v215 op_sel:[0,0,1]
	v_cvt_pk_fp8_f32 v74, v218, v219 op_sel:[0,0,1]
	s_nop 1
	v_mfma_f32_16x16x32_fp8_fp8 v[152:155], v[72:73], v[30:31], 0
	v_mfma_f32_16x16x32_fp8_fp8 v[152:155], v[74:75], v[32:33], v[152:155]
	v_fma_f32 v111, v105, v121, -v123
	v_exp_f32_e32 v111, v111
	s_nop 0
	v_mul_f32_e32 v112, v111, v101
	v_mul_f32_e32 v110, v111, v108
	v_add_f32_e32 v114, v114, v111
	v_pk_mul_f32 v[222:223], v[222:223], v[112:113] op_sel_hi:[1,0]
	v_pk_mul_f32 v[224:225], v[224:225], v[112:113] op_sel_hi:[1,0]
	v_pk_mul_f32 v[226:227], v[226:227], v[112:113] op_sel_hi:[1,0]
	v_pk_mul_f32 v[228:229], v[228:229], v[112:113] op_sel_hi:[1,0]
	v_pk_mul_f32 v[230:231], v[230:231], v[112:113] op_sel_hi:[1,0]
	v_pk_mul_f32 v[232:233], v[232:233], v[112:113] op_sel_hi:[1,0]
	v_pk_mul_f32 v[234:235], v[234:235], v[112:113] op_sel_hi:[1,0]
	s_waitcnt vmcnt(11)
	v_add_f32_e32 v115, v115, v110
	v_fma_mix_f32 v116, v110, v66, v116 op_sel_hi:[0,1,0]
	v_fma_mix_f32 v117, v110, v66, v117 op_sel:[0,1,0] op_sel_hi:[0,1,0]
	v_fma_mix_f32 v118, v110, v67, v118 op_sel_hi:[0,1,0]
	v_cvt_pk_fp8_f32 v76, v222, v223
	v_cvt_pk_fp8_f32 v77, v226, v227
	v_cvt_pk_fp8_f32 v78, v230, v231
	v_cvt_pk_fp8_f32 v79, v234, v235
	v_cvt_pk_fp8_f32 v76, v224, v225 op_sel:[0,0,1]
	v_cvt_pk_fp8_f32 v77, v228, v229 op_sel:[0,0,1]
	v_cvt_pk_fp8_f32 v78, v232, v233 op_sel:[0,0,1]
	s_nop 1
	v_mfma_f32_16x16x32_fp8_fp8 v[152:155], v[76:77], v[26:27], v[152:155]
	v_mfma_f32_16x16x32_fp8_fp8 v[152:155], v[78:79], v[28:29], v[152:155]
	v_fma_f32 v111, v106, v121, -v123
	v_exp_f32_e32 v111, v111
	s_nop 0
	v_mul_f32_e32 v112, v111, v102
	v_mul_f32_e32 v110, v111, v109
	v_add_f32_e32 v114, v114, v111
	v_pk_mul_f32 v[236:237], v[236:237], v[112:113] op_sel_hi:[1,0]
	v_pk_mul_f32 v[238:239], v[238:239], v[112:113] op_sel_hi:[1,0]
	v_pk_mul_f32 v[240:241], v[240:241], v[112:113] op_sel_hi:[1,0]
	v_pk_mul_f32 v[242:243], v[242:243], v[112:113] op_sel_hi:[1,0]
	v_pk_mul_f32 v[244:245], v[244:245], v[112:113] op_sel_hi:[1,0]
	v_pk_mul_f32 v[246:247], v[246:247], v[112:113] op_sel_hi:[1,0]
	v_pk_mul_f32 v[248:249], v[248:249], v[112:113] op_sel_hi:[1,0]
	s_waitcnt vmcnt(9)
	v_add_f32_e32 v115, v115, v110
	v_fma_mix_f32 v116, v110, v68, v116 op_sel_hi:[0,1,0]
	v_fma_mix_f32 v117, v110, v68, v117 op_sel:[0,1,0] op_sel_hi:[0,1,0]
	v_fma_mix_f32 v118, v110, v69, v118 op_sel_hi:[0,1,0]
	v_cvt_pk_fp8_f32 v80, v236, v237
	v_cvt_pk_fp8_f32 v81, v240, v241
	v_cvt_pk_fp8_f32 v82, v244, v245
	v_cvt_pk_fp8_f32 v83, v248, v249
	v_cvt_pk_fp8_f32 v80, v238, v239 op_sel:[0,0,1]
	v_cvt_pk_fp8_f32 v81, v242, v243 op_sel:[0,0,1]
	v_cvt_pk_fp8_f32 v82, v246, v247 op_sel:[0,0,1]
	s_nop 1
	v_mfma_f32_16x16x32_fp8_fp8 v[152:155], v[80:81], v[18:19], v[152:155]
	v_mfma_f32_16x16x32_fp8_fp8 v[152:155], v[82:83], v[20:21], v[152:155]
	v_mov_b32_e32 v86, v114
	v_mov_b32_e32 v87, v115
	v_mov_b32_e32 v88, v116
	v_mov_b32_e32 v89, v117
	v_mov_b32_e32 v90, v118
	v_permlane16_swap_b32_e32 v114, v86
	v_permlane16_swap_b32_e32 v115, v87
	v_permlane16_swap_b32_e32 v116, v88
	v_permlane16_swap_b32_e32 v117, v89
	v_permlane16_swap_b32_e32 v118, v90
	v_add_f32_e32 v114, v114, v86
	v_add_f32_e32 v115, v115, v87
	v_add_f32_e32 v116, v116, v88
	v_add_f32_e32 v117, v117, v89
	v_add_f32_e32 v118, v118, v90
	v_mov_b32_e32 v86, v114
	v_mov_b32_e32 v87, v115
	v_mov_b32_e32 v88, v116
	v_mov_b32_e32 v89, v117
	v_mov_b32_e32 v90, v118
	v_permlane32_swap_b32_e32 v114, v86
	v_permlane32_swap_b32_e32 v115, v87
	v_permlane32_swap_b32_e32 v116, v88
	v_permlane32_swap_b32_e32 v117, v89
	v_permlane32_swap_b32_e32 v118, v90
	v_add_f32_e32 v37, v114, v86
	v_add_f32_e32 v20, v115, v87
	v_add_f32_e32 v18, v116, v88
	v_add_f32_e32 v19, v117, v89
	v_add_f32_e32 v21, v118, v90
	ds_write2_b32 v156, v152, v153 offset0:0 offset1:20
	ds_write2_b32 v156, v154, v155 offset0:40 offset1:60

.LBB1_16:
	s_mov_b32 exec_lo, 0x1ff01ff
	s_mov_b32 exec_hi, 0x1ff01ff
	global_load_dword v120, v144, s[10:11]
	s_mov_b32 exec_lo, 0xe000e00
	s_mov_b32 exec_hi, 0xe000e00
	global_load_dword v120, v145, s[12:13]
	s_mov_b32 exec_lo, 0x70007000
	s_mov_b32 exec_hi, 0x70007000
	global_load_dword v120, v146, s[14:15]
	s_mov_b64 exec, -1
	global_load_dwordx4 v[124:127], v147, s[22:23]
	global_load_dwordx4 v[128:131], v148, s[22:23]
	s_mov_b32 exec_hi, 0
	global_load_dwordx4 v[132:135], v149, s[16:17]
	s_mov_b32 exec_hi, -1
	s_mov_b32 exec_lo, 0
	global_load_dwordx4 v[132:135], v149, s[18:19] offset:-512
	s_mov_b32 exec_lo, -1
	global_load_dwordx4 v[136:139], v150, s[8:9]
	global_load_dwordx4 v[140:143], v150, s[8:9] offset:256
	v_mov_b32_e32 v21, 0
	ds_write2_b32 v156, v21, v21 offset1:20
	ds_write2_b32 v156, v21, v21 offset0:40 offset1:60
	v_cmp_gt_u32_e64 s[6:7], 16, v104
	v_mov_b32_e32 v37, 1.0
	v_mov_b32_e32 v20, 0
	v_mov_b32_e32 v19, 0
	v_mov_b32_e32 v18, 0
	v_mov_b32_e32 v36, 0
	s_branch .LBB1_30
